# speedup vs baseline: 1.0062x; 1.0062x over previous
_Z6k_attnILi1024ELi1024ELi1024ELi1024ELi3072ELi1024ELb1ELb1EEvPKDF16_S1_S1_PKfPDF16_:
	s_load_dwordx8 s[8:15], s[0:1], 0x0
	s_load_dwordx2 s[16:17], s[0:1], 0x20
	s_lshl_b32 s0, s2, 1
	s_and_b32 s24, s0, 14
	s_lshr_b32 s0, s2, 7
	s_add_i32 s24, s24, s0
	v_readfirstlane_b32 s40, v0
	s_lshr_b32 s0, s24, 2
	s_lshr_b32 s33, s40, 6
	s_mov_b32 s1, 0
	s_lshl_b32 s3, s2, 3
	s_lshr_b32 s4, s40, 2
	s_lshr_b32 s55, s2, 3
	s_and_b32 s55, s55, 7
	s_lshl_b32 s55, s55, 1
	s_lshr_b32 s6, s33, 2
	s_add_i32 s6, s6, s55
	s_lshl_b32 s6, s6, 6
	s_lshr_b32 s57, s33, 2
	s_lshl_b32 s57, s57, 12
	s_lshr_b32 s61, s33, 2
	s_mul_i32 s61, s61, 0x6800
	s_mov_b64 s[58:59], 0x80
	s_lshl_b64 s[20:21], s[0:1], 20
	s_and_b32 s3, s4, 48
	s_lshl_b32 s35, s33, 10
	s_cmp_lg_u32 0, -1
	s_cselect_b32 s5, 0, 0
	s_add_i32 s37, s35, s5
	s_waitcnt lgkmcnt(0)
	s_mov_b64 s[70:71], s[14:15]
	s_add_u32 s5, s10, s20
	v_bfe_u32 v202, v0, 2, 4
	s_addc_u32 s19, s11, s21
	v_or_b32_e32 v20, s3, v202
	s_add_u32 s18, s5, s6
	v_bfe_u32 v30, v0, 4, 2
	s_addc_u32 s19, s19, 0
	v_lshlrev_b32_e32 v18, 10, v20
	v_mov_b32_e32 v19, 0
	v_bitop3_b32 v1, v30, v0, 3 bitop3:0x78
	v_lshl_add_u64 v[2:3], s[18:19], 0, v[18:19]
	v_lshlrev_b32_e32 v18, 4, v1
	s_cmpk_lt_u32 s40, 0x100
	s_mov_b32 s7, s1
	v_and_b32_e32 v24, 3, v0
	s_cselect_b64 s[18:19], -1, 0
	s_cmpk_gt_u32 s40, 0xff
	v_lshl_add_u64 v[22:23], v[2:3], 0, v[18:19]
	s_nop 0
	s_mov_b32 m0, s37
	s_nop 0
	global_load_lds_dwordx4 v[22:23], off

.LBB3_8:
	v_lshl_add_u64 v[178:179], v[24:25], 0, s[0:1]
	s_and_b32 s0, s40, 0x3fffffc0
	s_lshl_b32 s0, s0, 2
	s_add_i32 s23, s0, 0
	s_add_i32 s0, s7, 0
	s_add_i32 s0, s0, 0x14800
	v_lshlrev_b32_e32 v0, 8, v0
	s_cmp_lg_u32 0, -1
	v_lshl_add_u64 v[174:175], v[28:29], 0, s[24:25]
	v_exp_f32_e32 v80, v64
	v_exp_f32_e32 v64, v2
	v_lshlrev_b32_e32 v2, 10, v106
	v_and_b32_e32 v0, 0x300, v0
	s_cselect_b32 s24, 0, 0
	v_add3_u32 v222, s0, v2, v0
	s_add_i32 s0, s24, s35
	s_add_i32 s24, s24, s7
	v_lshl_add_u64 v[166:167], v[28:29], 0, s[30:31]
	s_add_i32 s0, s0, 0x8000
	s_add_i32 s30, s24, 0x14c00
	s_add_i32 s31, s24, 0x15000
	s_add_i32 s40, s24, 0x15400
	s_add_i32 s41, s24, 0x15800
	s_add_i32 s42, s24, 0x15c00
	s_add_i32 s43, s24, 0x16000
	s_add_i32 s44, s24, 0x16400
	v_lshlrev_b32_e32 v0, 5, v30
	v_lshrrev_b32_e32 v2, 2, v105
	s_add_u32 s20, s6, s20
	v_and_b32_e32 v0, 32, v0
	v_or_b32_e32 v2, v31, v2
	s_addc_u32 s21, 0, s21
	s_lshl_b32 s2, s55, 7
	v_lshl_add_u64 v[176:177], v[26:27], 0, s[8:9]
	v_add_u32_e32 v0, 0, v0
	v_lshlrev_b32_e32 v2, 6, v2
	s_mov_b64 s[8:9], 0x60000
	s_and_b32 s2, s2, 0x780
	v_exp_f32_e32 v81, v65
	v_exp_f32_e32 v65, v3
	v_add3_u32 v207, v0, v104, v2
	v_add_u32_e32 v207, s61, v207
	v_lshl_add_u64 v[2:3], v[162:163], 0, s[8:9]
	s_mov_b32 m0, s0
	s_nop 0
	global_load_lds_dwordx4 v[2:3], off
	v_lshl_add_u64 v[226:227], v[2:3], 0, s[58:59]
	s_add_i32 m0, s0, 0x6800
	s_nop 0
	global_load_lds_dwordx4 v[226:227], off
	v_add_lshl_u32 v184, v202, s3, 10
	v_mov_b32_e32 v185, 0
	s_add_u32 s2, s22, s2
	v_exp_f32_e32 v82, v66
	v_exp_f32_e32 v66, v4
	v_xor_b32_e32 v4, v204, v105
	ds_read_b128 v[112:115], v209 offset:8192
	ds_read_b128 v[104:107], v209 offset:10240
	ds_read_b128 v[116:119], v210 offset:8192
	ds_read_b128 v[108:111], v210 offset:10240
	v_cmp_gt_u32_e64 s[0:1], 32, v1
	v_lshl_add_u64 v[0:1], s[20:21], 0, v[184:185]
	s_addc_u32 s3, 0, 0
	v_lshl_add_u64 v[0:1], v[0:1], 0, v[18:19]
	s_add_u32 s2, s2, s46
	v_lshl_add_u64 v[0:1], s[10:11], 0, v[0:1]
	s_addc_u32 s3, s3, s45
	v_exp_f32_e32 v83, v67
	v_exp_f32_e32 v67, v5
	v_exp_f32_e32 v84, v68
	v_exp_f32_e32 v68, v6
	v_exp_f32_e32 v85, v69
	v_exp_f32_e32 v69, v7
	v_exp_f32_e32 v86, v70
	v_exp_f32_e32 v70, v8
	v_exp_f32_e32 v87, v71
	v_exp_f32_e32 v71, v9
	v_exp_f32_e32 v88, v72
	v_exp_f32_e32 v72, v10
	v_exp_f32_e32 v89, v73
	v_exp_f32_e32 v73, v11
	v_exp_f32_e32 v90, v74
	v_exp_f32_e32 v74, v12
	v_exp_f32_e32 v91, v75
	v_exp_f32_e32 v75, v13
	v_exp_f32_e32 v92, v76
	v_exp_f32_e32 v76, v14
	v_exp_f32_e32 v93, v77
	v_exp_f32_e32 v77, v94
	v_exp_f32_e32 v94, v78
	v_exp_f32_e32 v78, v16
	v_exp_f32_e32 v95, v79
	v_exp_f32_e32 v79, v15
	v_lshl_add_u64 v[180:181], v[0:1], 0, s[14:15]
	v_lshl_add_u64 v[0:1], s[2:3], 0, v[20:21]
	v_mov_b32_e32 v161, v185
	s_waitcnt vmcnt(3) lgkmcnt(0)
	s_barrier
	v_lshlrev_b32_e32 v223, 4, v4
	v_lshl_add_u64 v[0:1], v[0:1], 0, v[160:161]
	v_xor_b32_e32 v2, 0x80, v223
	v_xor_b32_e32 v3, 32, v223
	v_xor_b32_e32 v4, 0xa0, v223
	v_xor_b32_e32 v5, 64, v223
	v_xor_b32_e32 v6, 0xc0, v223
	v_xor_b32_e32 v7, 0x60, v223
	v_xor_b32_e32 v8, 0xe0, v223
	v_lshl_add_u64 v[0:1], s[12:13], 0, v[0:1]
	v_lshl_add_u64 v[172:173], v[164:165], 0, s[14:15]
	v_lshl_add_u64 v[170:171], v[24:25], 0, s[26:27]
	v_lshl_add_u64 v[168:169], v[26:27], 0, s[28:29]
	v_lshl_add_u32 v206, v203, 2, s23
	v_lshl_add_u32 v205, v31, 2, s23
	v_lshl_add_u64 v[182:183], v[0:1], 0, s[8:9]
	s_movk_i32 s45, 0x4000
	s_movk_i32 s47, 0x2000
	s_mov_b64 s[2:3], 0
	s_mov_b32 s46, 0x41000000
	s_mov_b64 s[10:11], 0x30000
	s_mov_b64 s[12:13], 0x300
	s_mov_b64 s[14:15], 0x40000
	s_mov_b64 s[20:21], 0xc0000
	s_mov_b64 s[22:23], 0x400
	s_mov_b64 s[24:25], 0x20000
	v_add_u32_e32 v161, v222, v2
	v_add_u32_e32 v184, v222, v3
	v_add_u32_e32 v211, v222, v4
	v_add_u32_e32 v212, v222, v5
	v_add_u32_e32 v213, v222, v6
	v_add_u32_e32 v214, v222, v7
	v_add_u32_e32 v215, v222, v8
	v_mov_b32_e32 v0, v185
	v_mov_b32_e32 v1, v185
	v_mov_b32_e32 v2, v185
	v_mov_b32_e32 v3, v185
	v_mov_b32_e32 v4, v185
	v_mov_b32_e32 v5, v185
	v_mov_b32_e32 v6, v185
	v_mov_b32_e32 v7, v185
	v_mov_b32_e32 v8, v185
	v_mov_b32_e32 v9, v185
	v_mov_b32_e32 v10, v185
	v_mov_b32_e32 v11, v185
	v_mov_b32_e32 v12, v185
	v_mov_b32_e32 v13, v185
	v_mov_b32_e32 v14, v185
	v_mov_b32_e32 v15, v185
	v_mov_b32_e32 v16, v185
	v_mov_b32_e32 v17, v185
	v_mov_b32_e32 v18, v185
	v_mov_b32_e32 v19, v185
	v_mov_b32_e32 v20, v185
	v_mov_b32_e32 v21, v185
	v_mov_b32_e32 v22, v185
	v_mov_b32_e32 v23, v185
	v_mov_b32_e32 v24, v185
	v_mov_b32_e32 v25, v185
	v_mov_b32_e32 v26, v185
	v_mov_b32_e32 v27, v185
	v_mov_b32_e32 v28, v185
	v_mov_b32_e32 v29, v185
	v_mov_b32_e32 v30, v185
	v_mov_b32_e32 v31, v185
	v_add_u32_e32 v221, v222, v223
	v_subrev_u32_e32 v230, s70, v164
	v_add_u32_e32 v230, s62, v230
	v_subrev_u32_e32 v231, s70, v178
	v_add_u32_e32 v231, s62, v231
	v_subrev_u32_e32 v232, s70, v176
	v_add_u32_e32 v232, s62, v232
	v_subrev_u32_e32 v233, s70, v174
	v_add_u32_e32 v233, s62, v233
.LBB3_9:
	s_add_u32 s68, s70, s2
	s_addc_u32 s69, s71, s3
	s_add_u32 s68, s68, s12
	s_addc_u32 s69, s69, s13
	v_add_u32_e32 v138, s48, v207
	ds_read_b64_tr_b16 v[156:157], v138 offset:24576
	ds_read_b64_tr_b16 v[158:159], v138 offset:25088
	v_add_f32_e32 v120, v80, v81
	s_waitcnt lgkmcnt(3)
	v_mfma_scale_f32_32x32x64_f8f6f4 v[48:63], v[112:119], v[96:103], v[48:63], v219, v220 op_sel_hi:[0,0,0]
	v_add_f32_e32 v112, v82, v120
	v_add_f32_e32 v112, v83, v112
	v_add_f32_e32 v112, v84, v112
	v_add_f32_e32 v116, v85, v112
	v_cvt_pk_f16_f32 v132, v80, v81
	v_cvt_pk_f16_f32 v133, v82, v83
	ds_read_b64_tr_b16 v[112:113], v138 offset:28672
	ds_read_b64_tr_b16 v[114:115], v138 offset:29184
	v_add_f32_e32 v80, v86, v116
	v_add_f32_e32 v80, v87, v80
	v_add_f32_e32 v80, v88, v80
	v_add_f32_e32 v80, v89, v80
	v_cvt_pk_f16_f32 v134, v84, v85
	v_cvt_pk_f16_f32 v135, v86, v87
	s_waitcnt lgkmcnt(4)
	v_mfma_scale_f32_32x32x64_f8f6f4 v[32:47], v[104:111], v[96:103], v[32:47], v219, v220 op_sel_hi:[0,0,0]
	s_add_i32 m0, s36, s65
	s_nop 0
	global_load_lds_dwordx4 v230, s[68:69] nt
	ds_read_b64_tr_b16 v[104:105], v138 offset:25600
	ds_read_b64_tr_b16 v[106:107], v138 offset:26112
	s_add_i32 m0, s30, s65
	s_nop 0
	global_load_lds_dwordx4 v231, s[68:69] nt
	v_add_f32_e32 v80, v90, v80
	v_add_f32_e32 v80, v91, v80
	v_add_f32_e32 v80, v92, v80
	v_add_f32_e32 v80, v93, v80
	v_cvt_pk_f16_f32 v128, v88, v89
	v_cvt_pk_f16_f32 v129, v90, v91
	ds_read_b64_tr_b16 v[152:153], v138 offset:29696
	ds_read_b64_tr_b16 v[154:155], v138 offset:30208
	s_add_i32 m0, s31, s65
	s_nop 0
	global_load_lds_dwordx4 v232, s[68:69] nt
	v_add_f32_e32 v80, v94, v80
	v_add_f32_e32 v80, v95, v80
	v_add_f32_e32 v80, v64, v80
	v_add_f32_e32 v80, v65, v80
	v_cvt_pk_f16_f32 v130, v92, v93
	v_cvt_pk_f16_f32 v131, v94, v95
	ds_read_b64_tr_b16 v[148:149], v138 offset:26624
	ds_read_b64_tr_b16 v[150:151], v138 offset:27136
	s_add_i32 m0, s40, s65
	s_nop 0
	global_load_lds_dwordx4 v233, s[68:69] nt
	v_add_f32_e32 v80, v66, v80
	v_add_f32_e32 v80, v67, v80
	v_add_f32_e32 v80, v68, v80
	v_add_f32_e32 v80, v69, v80
	v_cvt_pk_f16_f32 v124, v64, v65
	v_cvt_pk_f16_f32 v125, v66, v67
	ds_read_b64_tr_b16 v[144:145], v138 offset:30720
	ds_read_b64_tr_b16 v[146:147], v138 offset:31232
	v_add_f32_e32 v64, v70, v80
	v_add_f32_e32 v64, v71, v64
	v_add_f32_e32 v64, v72, v64
	v_add_f32_e32 v64, v73, v64
	v_cvt_pk_f16_f32 v126, v68, v69
	v_cvt_pk_f16_f32 v127, v70, v71
	ds_read_b64_tr_b16 v[140:141], v138 offset:27648
	ds_read_b64_tr_b16 v[142:143], v138 offset:28160
	v_add_f32_e32 v64, v74, v64
	v_add_f32_e32 v64, v75, v64
	v_add_f32_e32 v64, v76, v64
	v_add_f32_e32 v64, v77, v64
	v_cvt_pk_f16_f32 v120, v72, v73
	v_cvt_pk_f16_f32 v121, v74, v75
	ds_read_b64_tr_b16 v[136:137], v138 offset:31744
	ds_read_b64_tr_b16 v[138:139], v138 offset:32256
	v_add_f32_e32 v64, v78, v64
	v_add_f32_e32 v64, v79, v64
	v_add_f32_e32 v108, 0, v64
	v_cvt_pk_f16_f32 v122, v76, v77
	v_cvt_pk_f16_f32 v123, v78, v79
	s_nop 1
	s_nop 0
	v_add_f32_e32 v185, v185, v108
	v_max_f32_e32 v108, v49, v49
	v_max_f32_e32 v109, v48, v48
	v_max_f32_e32 v108, v109, v108
	v_max3_f32 v109, v50, v51, v33
	v_max3_f32 v108, v108, v32, v34
	v_max3_f32 v108, v108, v35, v52
	v_max3_f32 v109, v109, v54, v55
	v_max3_f32 v108, v108, v53, v36
	v_max3_f32 v109, v109, v38, v39
	v_max3_f32 v108, v108, v37, v56
	v_max3_f32 v109, v109, v58, v59
	v_add_u32_e32 v221, v222, v223
	v_max3_f32 v108, v108, v57, v40
	v_max3_f32 v109, v109, v42, v43
	ds_read_b128 v[80:83], v221
	ds_read_b128 v[64:67], v161
	ds_read_b128 v[84:87], v184
	ds_read_b128 v[68:71], v211
	ds_read_b128 v[88:91], v212
	ds_read_b128 v[72:75], v213
	ds_read_b128 v[92:95], v214
	ds_read_b128 v[76:79], v215
	v_max3_f32 v108, v108, v41, v60
	v_max3_f32 v109, v109, v62, v63
	v_max3_f32 v108, v108, v61, v44
	v_max3_f32 v109, v109, v46, v47
	v_max3_f32 v108, v108, v45, v109
	v_mov_b32_e32 v109, v108
	s_nop 1
	v_permlane32_swap_b32_e32 v108, v109
	v_max_f32_e32 v109, v109, v109
	v_max_f32_e32 v108, v108, v108
	v_max_f32_e32 v108, v108, v109
	v_fma_f32 v108, v108, s39, -v208
	v_cmp_lt_f32_e32 vcc, s46, v108
	s_cmp_lg_u64 vcc, 0
	s_cselect_b64 s[26:27], -1, 0
	s_cbranch_vccnz .LBB3_21

.LBB3_14:
	s_add_u32 s68, s70, s2
	s_addc_u32 s69, s71, s3
	s_add_u32 s68, s68, s22
	s_addc_u32 s69, s69, s23
	v_add_u32_e32 v138, s47, v207
	ds_read_b64_tr_b16 v[156:157], v138 offset:24576
	ds_read_b64_tr_b16 v[158:159], v138 offset:25088
	v_add_f32_e32 v120, v48, v49
	s_waitcnt lgkmcnt(4)
	v_mfma_scale_f32_32x32x64_f8f6f4 v[80:95], v[112:119], v[96:103], v[80:95], v219, v220 op_sel_hi:[0,0,0]
	v_add_f32_e32 v112, v50, v120
	v_add_f32_e32 v112, v51, v112
	v_add_f32_e32 v112, v52, v112
	v_add_f32_e32 v116, v53, v112
	v_cvt_pk_f16_f32 v132, v48, v49
	v_cvt_pk_f16_f32 v133, v50, v51
	ds_read_b64_tr_b16 v[112:113], v138 offset:28672
	ds_read_b64_tr_b16 v[114:115], v138 offset:29184
	v_add_f32_e32 v48, v54, v116
	v_add_f32_e32 v48, v55, v48
	v_add_f32_e32 v48, v56, v48
	v_add_f32_e32 v48, v57, v48
	v_cvt_pk_f16_f32 v134, v52, v53
	v_cvt_pk_f16_f32 v135, v54, v55
	s_waitcnt lgkmcnt(4)
	v_mfma_scale_f32_32x32x64_f8f6f4 v[64:79], v[104:111], v[96:103], v[64:79], v219, v220 op_sel_hi:[0,0,0]
	s_add_i32 m0, s36, s64
	s_nop 0
	global_load_lds_dwordx4 v230, s[68:69] nt
	ds_read_b64_tr_b16 v[104:105], v138 offset:25600
	ds_read_b64_tr_b16 v[106:107], v138 offset:26112
	s_add_i32 m0, s30, s64
	s_nop 0
	global_load_lds_dwordx4 v231, s[68:69] nt
	v_add_f32_e32 v48, v58, v48
	v_add_f32_e32 v48, v59, v48
	v_add_f32_e32 v48, v60, v48
	v_add_f32_e32 v48, v61, v48
	v_cvt_pk_f16_f32 v128, v56, v57
	v_cvt_pk_f16_f32 v129, v58, v59
	ds_read_b64_tr_b16 v[152:153], v138 offset:29696
	ds_read_b64_tr_b16 v[154:155], v138 offset:30208
	s_add_i32 m0, s31, s64
	s_nop 0
	global_load_lds_dwordx4 v232, s[68:69] nt
	v_add_f32_e32 v48, v62, v48
	v_add_f32_e32 v48, v63, v48
	v_add_f32_e32 v48, v32, v48
	v_add_f32_e32 v48, v33, v48
	v_cvt_pk_f16_f32 v130, v60, v61
	v_cvt_pk_f16_f32 v131, v62, v63
	ds_read_b64_tr_b16 v[148:149], v138 offset:26624
	ds_read_b64_tr_b16 v[150:151], v138 offset:27136
	s_add_i32 m0, s40, s64
	s_nop 0
	global_load_lds_dwordx4 v233, s[68:69] nt
	v_add_f32_e32 v48, v34, v48
	v_add_f32_e32 v48, v35, v48
	v_add_f32_e32 v48, v36, v48
	v_add_f32_e32 v48, v37, v48
	v_cvt_pk_f16_f32 v124, v32, v33
	v_cvt_pk_f16_f32 v125, v34, v35
	ds_read_b64_tr_b16 v[144:145], v138 offset:30720
	ds_read_b64_tr_b16 v[146:147], v138 offset:31232
	v_add_f32_e32 v32, v38, v48
	v_add_f32_e32 v32, v39, v32
	v_add_f32_e32 v32, v40, v32
	v_add_f32_e32 v32, v41, v32
	v_cvt_pk_f16_f32 v126, v36, v37
	v_cvt_pk_f16_f32 v127, v38, v39
	ds_read_b64_tr_b16 v[140:141], v138 offset:27648
	ds_read_b64_tr_b16 v[142:143], v138 offset:28160
	v_add_f32_e32 v32, v42, v32
	v_add_f32_e32 v32, v43, v32
	v_add_f32_e32 v32, v44, v32
	v_add_f32_e32 v32, v45, v32
	v_cvt_pk_f16_f32 v120, v40, v41
	v_cvt_pk_f16_f32 v121, v42, v43
	ds_read_b64_tr_b16 v[136:137], v138 offset:31744
	ds_read_b64_tr_b16 v[138:139], v138 offset:32256
	v_add_f32_e32 v32, v46, v32
	v_add_f32_e32 v32, v47, v32
	v_add_f32_e32 v108, 0, v32
	v_cvt_pk_f16_f32 v122, v44, v45
	v_cvt_pk_f16_f32 v123, v46, v47
	s_nop 1
	s_nop 0
	v_add_f32_e32 v185, v185, v108
	v_max_f32_e32 v108, v81, v81
	v_max_f32_e32 v109, v80, v80
	v_max_f32_e32 v108, v109, v108
	v_max3_f32 v109, v82, v83, v65
	v_max3_f32 v108, v108, v64, v66
	v_max3_f32 v108, v108, v67, v84
	v_max3_f32 v109, v109, v86, v87
	v_max3_f32 v108, v108, v85, v68
	v_max3_f32 v109, v109, v70, v71
	v_max3_f32 v108, v108, v69, v88
	v_max3_f32 v109, v109, v90, v91
	v_max3_f32 v108, v108, v89, v72
	v_max3_f32 v109, v109, v74, v75
	ds_read_b128 v[48:51], v221 offset:32768
	ds_read_b128 v[32:35], v161 offset:32768
	ds_read_b128 v[52:55], v184 offset:32768
	ds_read_b128 v[36:39], v211 offset:32768
	ds_read_b128 v[56:59], v212 offset:32768
	ds_read_b128 v[40:43], v213 offset:32768
	ds_read_b128 v[60:63], v214 offset:32768
	ds_read_b128 v[44:47], v215 offset:32768
	v_max3_f32 v108, v108, v73, v92
	v_max3_f32 v109, v109, v94, v95
	v_max3_f32 v108, v108, v93, v76
	v_max3_f32 v109, v109, v78, v79
	v_max3_f32 v108, v108, v77, v109
	v_mov_b32_e32 v109, v108
	s_nop 1
	v_permlane32_swap_b32_e32 v108, v109
	v_max_f32_e32 v109, v109, v109
	v_max_f32_e32 v108, v108, v108
	v_max_f32_e32 v108, v108, v109
	v_fma_f32 v108, v108, s39, -v208
	v_cmp_lt_f32_e32 vcc, s46, v108
	s_cmp_lg_u64 vcc, 0
	s_cselect_b64 s[26:27], -1, 0
	s_cbranch_vccnz .LBB3_24

	.amdhsa_kernel _Z6k_attnILi1024ELi1024ELi1024ELi1024ELi3072ELi1024ELb1ELb1EEvPKDF16_S1_S1_PKfPDF16_
		.amdhsa_group_segment_fixed_size 0
		.amdhsa_private_segment_fixed_size 0
		.amdhsa_kernarg_size 40
		.amdhsa_user_sgpr_count 2
		.amdhsa_user_sgpr_dispatch_ptr 0
		.amdhsa_user_sgpr_queue_ptr 0
		.amdhsa_user_sgpr_kernarg_segment_ptr 1
		.amdhsa_user_sgpr_dispatch_id 0
		.amdhsa_user_sgpr_kernarg_preload_length 0
		.amdhsa_user_sgpr_kernarg_preload_offset 0
		.amdhsa_user_sgpr_private_segment_size 0
		.amdhsa_uses_dynamic_stack 0
		.amdhsa_enable_private_segment 0
		.amdhsa_system_sgpr_workgroup_id_x 1
		.amdhsa_system_sgpr_workgroup_id_y 0
		.amdhsa_system_sgpr_workgroup_id_z 0
		.amdhsa_system_sgpr_workgroup_info 0
		.amdhsa_system_vgpr_workitem_id 0
		.amdhsa_next_free_vgpr 240
		.amdhsa_next_free_sgpr 72
		.amdhsa_accum_offset 240
		.amdhsa_reserve_vcc 1
		.amdhsa_float_round_mode_32 0
		.amdhsa_float_round_mode_16_64 0
		.amdhsa_float_denorm_mode_32 3
		.amdhsa_float_denorm_mode_16_64 3
		.amdhsa_dx10_clamp 1
		.amdhsa_ieee_mode 1
		.amdhsa_fp16_overflow 0
		.amdhsa_tg_split 0
		.amdhsa_exception_fp_ieee_invalid_op 0
		.amdhsa_exception_fp_denorm_src 0
		.amdhsa_exception_fp_ieee_div_zero 0
		.amdhsa_exception_fp_ieee_overflow 0
		.amdhsa_exception_fp_ieee_underflow 0
		.amdhsa_exception_fp_ieee_inexact 0
		.amdhsa_exception_int_div_zero 0
	.end_amdhsa_kernel

_Z6k_attnILi1024ELi2048ELi1024ELi1024ELi2048ELi1024ELb1ELb1EEvPKDF16_S1_S1_PKfPDF16_:
	s_load_dwordx8 s[8:15], s[0:1], 0x0
	s_load_dwordx2 s[16:17], s[0:1], 0x20
	s_lshl_b32 s0, s2, 1
	s_and_b32 s20, s0, 14
	s_lshr_b32 s0, s2, 7
	s_add_i32 s20, s20, s0
	v_readfirstlane_b32 s42, v0
	s_lshr_b32 s0, s20, 2
	s_lshr_b32 s33, s42, 6
	s_mov_b32 s1, 0
	s_lshl_b32 s3, s2, 3
	s_lshr_b32 s4, s42, 2
	s_lshr_b32 s55, s2, 3
	s_and_b32 s55, s55, 7
	s_lshl_b32 s55, s55, 1
	s_lshr_b32 s6, s33, 2
	s_add_i32 s6, s6, s55
	s_lshl_b32 s6, s6, 6
	s_lshr_b32 s57, s33, 2
	s_lshl_b32 s57, s57, 12
	s_lshr_b32 s61, s33, 2
	s_mul_i32 s61, s61, 0x6800
	s_mov_b64 s[58:59], 0x80
	s_lshl_b64 s[22:23], s[0:1], 21
	s_and_b32 s3, s4, 48
	s_lshl_b32 s36, s33, 10
	s_cmp_lg_u32 0, -1
	s_cselect_b32 s5, 0, 0
	s_add_i32 s39, s36, s5
	s_waitcnt lgkmcnt(0)
	s_mov_b64 s[70:71], s[14:15]
	s_add_u32 s5, s10, s22
	v_bfe_u32 v202, v0, 2, 4
	s_addc_u32 s19, s11, s23
	v_or_b32_e32 v2, s3, v202
	s_add_u32 s18, s5, s6
	v_bfe_u32 v28, v0, 4, 2
	v_mov_b32_e32 v19, 0
	s_addc_u32 s19, s19, 0
	v_lshlrev_b32_e32 v18, 10, v2
	v_bitop3_b32 v1, v28, v0, 3 bitop3:0x78
	v_lshl_add_u64 v[4:5], s[18:19], 0, v[18:19]
	v_lshlrev_b32_e32 v18, 4, v1
	s_cmpk_lt_u32 s42, 0x100
	s_mov_b32 s7, s1
	v_and_b32_e32 v22, 3, v0
	s_cselect_b64 s[18:19], -1, 0
	s_cmpk_gt_u32 s42, 0xff
	v_lshl_add_u64 v[20:21], v[4:5], 0, v[18:19]
	s_nop 0
	s_mov_b32 m0, s39
	s_nop 0
	global_load_lds_dwordx4 v[20:21], off

.LBB6_8:
	v_lshl_add_u64 v[178:179], v[22:23], 0, s[0:1]
	s_and_b32 s0, s42, 0x3fffffc0
	s_lshl_b32 s0, s0, 2
	s_add_i32 s45, s0, 0
	s_add_i32 s0, s7, 0
	s_add_i32 s0, s0, 0x14800
	v_lshlrev_b32_e32 v0, 8, v0
	s_cmp_lg_u32 0, -1
	v_lshl_add_u64 v[170:171], v[22:23], 0, s[30:31]
	v_exp_f32_e32 v80, v64
	v_exp_f32_e32 v64, v2
	v_lshlrev_b32_e32 v2, 10, v104
	v_and_b32_e32 v0, 0x300, v0
	s_cselect_b32 s30, 0, 0
	v_add3_u32 v222, s0, v2, v0
	s_add_i32 s0, s30, s36
	s_add_i32 s44, s30, s7
	v_lshl_add_u64 v[166:167], v[26:27], 0, s[34:35]
	s_add_i32 s0, s0, 0x8000
	s_add_i32 s30, s44, 0x14c00
	s_add_i32 s31, s44, 0x15000
	s_add_i32 s34, s44, 0x15400
	s_add_i32 s35, s44, 0x15800
	s_add_i32 s42, s44, 0x15c00
	s_add_i32 s43, s44, 0x16000
	s_add_i32 s44, s44, 0x16400
	v_lshlrev_b32_e32 v0, 5, v28
	v_lshrrev_b32_e32 v2, 2, v31
	s_add_u32 s22, s6, s22
	v_and_b32_e32 v0, 32, v0
	v_or_b32_e32 v2, v29, v2
	s_addc_u32 s23, 0, s23
	s_lshl_b32 s2, s55, 7
	v_lshl_add_u64 v[174:175], v[26:27], 0, s[20:21]
	v_exp_f32_e32 v87, v71
	v_exp_f32_e32 v71, v9
	v_add_u32_e32 v0, 0, v0
	v_lshlrev_b32_e32 v2, 6, v2
	s_mov_b64 s[20:21], 0x40000
	v_add_u32_e32 v9, s3, v202
	s_and_b32 s2, s2, 0x780
	v_exp_f32_e32 v81, v65
	v_exp_f32_e32 v65, v3
	v_add3_u32 v207, v0, v30, v2
	v_add_u32_e32 v207, s61, v207
	v_lshl_add_u64 v[2:3], v[162:163], 0, s[20:21]
	s_mov_b32 m0, s0
	s_nop 0
	global_load_lds_dwordx4 v[2:3], off
	v_lshl_add_u64 v[226:227], v[2:3], 0, s[58:59]
	s_add_i32 m0, s0, 0x6800
	s_nop 0
	global_load_lds_dwordx4 v[226:227], off
	v_lshlrev_b32_e32 v184, 10, v9
	v_mov_b32_e32 v185, 0
	s_add_u32 s2, s26, s2
	ds_read_b128 v[112:115], v209 offset:8192
	ds_read_b128 v[104:107], v209 offset:10240
	ds_read_b128 v[116:119], v210 offset:8192
	ds_read_b128 v[108:111], v210 offset:10240
	v_cmp_gt_u32_e64 s[0:1], 32, v1
	v_lshl_add_u64 v[0:1], s[22:23], 0, v[184:185]
	s_addc_u32 s3, 0, 0
	v_lshl_add_u64 v[0:1], v[0:1], 0, v[18:19]
	s_add_u32 s2, s2, s24
	v_lshl_add_u64 v[0:1], s[10:11], 0, v[0:1]
	v_lshlrev_b32_e32 v184, 12, v9
	s_addc_u32 s3, s3, s25
	v_exp_f32_e32 v82, v66
	v_exp_f32_e32 v66, v4
	v_exp_f32_e32 v83, v67
	v_exp_f32_e32 v67, v5
	v_exp_f32_e32 v84, v68
	v_exp_f32_e32 v68, v6
	v_exp_f32_e32 v85, v69
	v_exp_f32_e32 v69, v7
	v_exp_f32_e32 v86, v70
	v_exp_f32_e32 v70, v8
	v_exp_f32_e32 v88, v72
	v_exp_f32_e32 v72, v10
	v_exp_f32_e32 v89, v73
	v_exp_f32_e32 v73, v11
	v_exp_f32_e32 v90, v74
	v_exp_f32_e32 v74, v12
	v_exp_f32_e32 v91, v75
	v_exp_f32_e32 v75, v13
	v_exp_f32_e32 v92, v76
	v_exp_f32_e32 v76, v14
	v_exp_f32_e32 v93, v77
	v_exp_f32_e32 v77, v94
	v_exp_f32_e32 v94, v78
	v_exp_f32_e32 v78, v16
	v_exp_f32_e32 v95, v79
	v_exp_f32_e32 v79, v15
	v_xor_b32_e32 v4, v204, v31
	v_lshl_add_u64 v[180:181], v[0:1], 0, s[28:29]
	v_lshl_add_u64 v[0:1], s[2:3], 0, v[184:185]
	v_mov_b32_e32 v161, v185
	s_waitcnt vmcnt(3) lgkmcnt(0)
	s_barrier
	v_lshlrev_b32_e32 v223, 4, v4
	v_lshl_add_u64 v[0:1], v[0:1], 0, v[160:161]
	v_xor_b32_e32 v2, 0x80, v223
	v_xor_b32_e32 v3, 32, v223
	v_xor_b32_e32 v4, 0xa0, v223
	v_xor_b32_e32 v5, 64, v223
	v_xor_b32_e32 v6, 0xc0, v223
	v_xor_b32_e32 v7, 0x60, v223
	v_xor_b32_e32 v8, 0xe0, v223
	v_lshl_add_u64 v[0:1], s[12:13], 0, v[0:1]
	v_lshl_add_u64 v[176:177], v[24:25], 0, s[28:29]
	v_lshl_add_u64 v[172:173], v[164:165], 0, s[8:9]
	v_lshl_add_u64 v[168:169], v[24:25], 0, s[14:15]
	v_lshl_add_u32 v206, v203, 2, s45
	v_lshl_add_u32 v205, v29, 2, s45
	v_lshl_add_u64 v[182:183], v[0:1], 0, s[20:21]
	s_movk_i32 s28, 0x4000
	s_movk_i32 s45, 0x2000
	s_mov_b64 s[2:3], 0
	s_mov_b32 s29, 0x41000000
	s_mov_b64 s[10:11], 0x300
	s_mov_b64 s[12:13], 0x80000
	s_mov_b64 s[22:23], 0x400
	v_add_u32_e32 v161, v222, v2
	v_add_u32_e32 v184, v222, v3
	v_add_u32_e32 v211, v222, v4
	v_add_u32_e32 v212, v222, v5
	v_add_u32_e32 v213, v222, v6
	v_add_u32_e32 v214, v222, v7
	v_add_u32_e32 v215, v222, v8
	v_mov_b32_e32 v0, v185
	v_mov_b32_e32 v1, v185
	v_mov_b32_e32 v2, v185
	v_mov_b32_e32 v3, v185
	v_mov_b32_e32 v4, v185
	v_mov_b32_e32 v5, v185
	v_mov_b32_e32 v6, v185
	v_mov_b32_e32 v7, v185
	v_mov_b32_e32 v8, v185
	v_mov_b32_e32 v9, v185
	v_mov_b32_e32 v10, v185
	v_mov_b32_e32 v11, v185
	v_mov_b32_e32 v12, v185
	v_mov_b32_e32 v13, v185
	v_mov_b32_e32 v14, v185
	v_mov_b32_e32 v15, v185
	v_mov_b32_e32 v16, v185
	v_mov_b32_e32 v17, v185
	v_mov_b32_e32 v18, v185
	v_mov_b32_e32 v19, v185
	v_mov_b32_e32 v20, v185
	v_mov_b32_e32 v21, v185
	v_mov_b32_e32 v22, v185
	v_mov_b32_e32 v23, v185
	v_mov_b32_e32 v24, v185
	v_mov_b32_e32 v25, v185
	v_mov_b32_e32 v26, v185
	v_mov_b32_e32 v27, v185
	v_mov_b32_e32 v28, v185
	v_mov_b32_e32 v29, v185
	v_mov_b32_e32 v30, v185
	v_mov_b32_e32 v31, v185
	v_add_u32_e32 v221, v222, v223
	v_subrev_u32_e32 v230, s70, v164
	v_add_u32_e32 v230, s62, v230
	v_subrev_u32_e32 v231, s70, v178
	v_add_u32_e32 v231, s62, v231
	v_subrev_u32_e32 v232, s70, v176
	v_add_u32_e32 v232, s62, v232
	v_subrev_u32_e32 v233, s70, v174
	v_add_u32_e32 v233, s62, v233
.LBB6_9:
	s_add_u32 s68, s70, s2
	s_addc_u32 s69, s71, s3
	s_add_u32 s68, s68, s10
	s_addc_u32 s69, s69, s11
	v_add_u32_e32 v138, s27, v207
	ds_read_b64_tr_b16 v[156:157], v138 offset:24576
	ds_read_b64_tr_b16 v[158:159], v138 offset:25088
	v_add_f32_e32 v120, v80, v81
	s_waitcnt lgkmcnt(3)
	v_mfma_scale_f32_32x32x64_f8f6f4 v[48:63], v[112:119], v[96:103], v[48:63], v219, v220 op_sel_hi:[0,0,0]
	v_add_f32_e32 v112, v82, v120
	v_add_f32_e32 v112, v83, v112
	v_add_f32_e32 v112, v84, v112
	v_add_f32_e32 v116, v85, v112
	v_cvt_pk_f16_f32 v132, v80, v81
	v_cvt_pk_f16_f32 v133, v82, v83
	ds_read_b64_tr_b16 v[112:113], v138 offset:28672
	ds_read_b64_tr_b16 v[114:115], v138 offset:29184
	v_add_f32_e32 v80, v86, v116
	v_add_f32_e32 v80, v87, v80
	v_add_f32_e32 v80, v88, v80
	v_add_f32_e32 v80, v89, v80
	v_cvt_pk_f16_f32 v134, v84, v85
	v_cvt_pk_f16_f32 v135, v86, v87
	s_waitcnt lgkmcnt(4)
	v_mfma_scale_f32_32x32x64_f8f6f4 v[32:47], v[104:111], v[96:103], v[32:47], v219, v220 op_sel_hi:[0,0,0]
	s_add_i32 m0, s38, s65
	s_nop 0
	global_load_lds_dwordx4 v230, s[68:69] nt
	ds_read_b64_tr_b16 v[104:105], v138 offset:25600
	ds_read_b64_tr_b16 v[106:107], v138 offset:26112
	s_add_i32 m0, s30, s65
	s_nop 0
	global_load_lds_dwordx4 v231, s[68:69] nt
	v_add_f32_e32 v80, v90, v80
	v_add_f32_e32 v80, v91, v80
	v_add_f32_e32 v80, v92, v80
	v_add_f32_e32 v80, v93, v80
	v_cvt_pk_f16_f32 v128, v88, v89
	v_cvt_pk_f16_f32 v129, v90, v91
	ds_read_b64_tr_b16 v[152:153], v138 offset:29696
	ds_read_b64_tr_b16 v[154:155], v138 offset:30208
	s_add_i32 m0, s31, s65
	s_nop 0
	global_load_lds_dwordx4 v232, s[68:69] nt
	v_add_f32_e32 v80, v94, v80
	v_add_f32_e32 v80, v95, v80
	v_add_f32_e32 v80, v64, v80
	v_add_f32_e32 v80, v65, v80
	v_cvt_pk_f16_f32 v130, v92, v93
	v_cvt_pk_f16_f32 v131, v94, v95
	ds_read_b64_tr_b16 v[148:149], v138 offset:26624
	ds_read_b64_tr_b16 v[150:151], v138 offset:27136
	s_add_i32 m0, s34, s65
	s_nop 0
	global_load_lds_dwordx4 v233, s[68:69] nt
	v_add_f32_e32 v80, v66, v80
	v_add_f32_e32 v80, v67, v80
	v_add_f32_e32 v80, v68, v80
	v_add_f32_e32 v80, v69, v80
	v_cvt_pk_f16_f32 v124, v64, v65
	v_cvt_pk_f16_f32 v125, v66, v67
	ds_read_b64_tr_b16 v[144:145], v138 offset:30720
	ds_read_b64_tr_b16 v[146:147], v138 offset:31232
	v_add_f32_e32 v64, v70, v80
	v_add_f32_e32 v64, v71, v64
	v_add_f32_e32 v64, v72, v64
	v_add_f32_e32 v64, v73, v64
	v_cvt_pk_f16_f32 v126, v68, v69
	v_cvt_pk_f16_f32 v127, v70, v71
	ds_read_b64_tr_b16 v[140:141], v138 offset:27648
	ds_read_b64_tr_b16 v[142:143], v138 offset:28160
	v_add_f32_e32 v64, v74, v64
	v_add_f32_e32 v64, v75, v64
	v_add_f32_e32 v64, v76, v64
	v_add_f32_e32 v64, v77, v64
	v_cvt_pk_f16_f32 v120, v72, v73
	v_cvt_pk_f16_f32 v121, v74, v75
	ds_read_b64_tr_b16 v[136:137], v138 offset:31744
	ds_read_b64_tr_b16 v[138:139], v138 offset:32256
	v_add_f32_e32 v64, v78, v64
	v_add_f32_e32 v64, v79, v64
	v_add_f32_e32 v108, 0, v64
	v_cvt_pk_f16_f32 v122, v76, v77
	v_cvt_pk_f16_f32 v123, v78, v79
	s_nop 1
	s_nop 0
	v_add_f32_e32 v185, v185, v108
	v_max_f32_e32 v108, v49, v49
	v_max_f32_e32 v109, v48, v48
	v_max_f32_e32 v108, v109, v108
	v_max3_f32 v109, v50, v51, v33
	v_max3_f32 v108, v108, v32, v34
	v_max3_f32 v108, v108, v35, v52
	v_max3_f32 v109, v109, v54, v55
	v_max3_f32 v108, v108, v53, v36
	v_max3_f32 v109, v109, v38, v39
	v_max3_f32 v108, v108, v37, v56
	v_max3_f32 v109, v109, v58, v59
	v_add_u32_e32 v221, v222, v223
	v_max3_f32 v108, v108, v57, v40
	v_max3_f32 v109, v109, v42, v43
	ds_read_b128 v[80:83], v221
	ds_read_b128 v[64:67], v161
	ds_read_b128 v[84:87], v184
	ds_read_b128 v[68:71], v211
	ds_read_b128 v[88:91], v212
	ds_read_b128 v[72:75], v213
	ds_read_b128 v[92:95], v214
	ds_read_b128 v[76:79], v215
	v_max3_f32 v108, v108, v41, v60
	v_max3_f32 v109, v109, v62, v63
	v_max3_f32 v108, v108, v61, v44
	v_max3_f32 v109, v109, v46, v47
	v_max3_f32 v108, v108, v45, v109
	v_mov_b32_e32 v109, v108
	s_nop 1
	v_permlane32_swap_b32_e32 v108, v109
	v_max_f32_e32 v109, v109, v109
	v_max_f32_e32 v108, v108, v108
	v_max_f32_e32 v108, v108, v109
	v_fma_f32 v108, v108, s41, -v208
	v_cmp_lt_f32_e32 vcc, s29, v108
	s_cmp_lg_u64 vcc, 0
	s_cselect_b64 s[24:25], -1, 0
	s_cbranch_vccnz .LBB6_21

.LBB6_14:
	s_add_u32 s68, s70, s2
	s_addc_u32 s69, s71, s3
	s_add_u32 s68, s68, s22
	s_addc_u32 s69, s69, s23
	v_add_u32_e32 v138, s45, v207
	ds_read_b64_tr_b16 v[156:157], v138 offset:24576
	ds_read_b64_tr_b16 v[158:159], v138 offset:25088
	v_add_f32_e32 v120, v48, v49
	s_waitcnt lgkmcnt(4)
	v_mfma_scale_f32_32x32x64_f8f6f4 v[80:95], v[112:119], v[96:103], v[80:95], v219, v220 op_sel_hi:[0,0,0]
	v_add_f32_e32 v112, v50, v120
	v_add_f32_e32 v112, v51, v112
	v_add_f32_e32 v112, v52, v112
	v_add_f32_e32 v116, v53, v112
	v_cvt_pk_f16_f32 v132, v48, v49
	v_cvt_pk_f16_f32 v133, v50, v51
	ds_read_b64_tr_b16 v[112:113], v138 offset:28672
	ds_read_b64_tr_b16 v[114:115], v138 offset:29184
	v_add_f32_e32 v48, v54, v116
	v_add_f32_e32 v48, v55, v48
	v_add_f32_e32 v48, v56, v48
	v_add_f32_e32 v48, v57, v48
	v_cvt_pk_f16_f32 v134, v52, v53
	v_cvt_pk_f16_f32 v135, v54, v55
	s_waitcnt lgkmcnt(4)
	v_mfma_scale_f32_32x32x64_f8f6f4 v[64:79], v[104:111], v[96:103], v[64:79], v219, v220 op_sel_hi:[0,0,0]
	s_add_i32 m0, s38, s64
	s_nop 0
	global_load_lds_dwordx4 v230, s[68:69] nt
	ds_read_b64_tr_b16 v[104:105], v138 offset:25600
	ds_read_b64_tr_b16 v[106:107], v138 offset:26112
	s_add_i32 m0, s30, s64
	s_nop 0
	global_load_lds_dwordx4 v231, s[68:69] nt
	v_add_f32_e32 v48, v58, v48
	v_add_f32_e32 v48, v59, v48
	v_add_f32_e32 v48, v60, v48
	v_add_f32_e32 v48, v61, v48
	v_cvt_pk_f16_f32 v128, v56, v57
	v_cvt_pk_f16_f32 v129, v58, v59
	ds_read_b64_tr_b16 v[152:153], v138 offset:29696
	ds_read_b64_tr_b16 v[154:155], v138 offset:30208
	s_add_i32 m0, s31, s64
	s_nop 0
	global_load_lds_dwordx4 v232, s[68:69] nt
	v_add_f32_e32 v48, v62, v48
	v_add_f32_e32 v48, v63, v48
	v_add_f32_e32 v48, v32, v48
	v_add_f32_e32 v48, v33, v48
	v_cvt_pk_f16_f32 v130, v60, v61
	v_cvt_pk_f16_f32 v131, v62, v63
	ds_read_b64_tr_b16 v[148:149], v138 offset:26624
	ds_read_b64_tr_b16 v[150:151], v138 offset:27136
	s_add_i32 m0, s34, s64
	s_nop 0
	global_load_lds_dwordx4 v233, s[68:69] nt
	v_add_f32_e32 v48, v34, v48
	v_add_f32_e32 v48, v35, v48
	v_add_f32_e32 v48, v36, v48
	v_add_f32_e32 v48, v37, v48
	v_cvt_pk_f16_f32 v124, v32, v33
	v_cvt_pk_f16_f32 v125, v34, v35
	ds_read_b64_tr_b16 v[144:145], v138 offset:30720
	ds_read_b64_tr_b16 v[146:147], v138 offset:31232
	v_add_f32_e32 v32, v38, v48
	v_add_f32_e32 v32, v39, v32
	v_add_f32_e32 v32, v40, v32
	v_add_f32_e32 v32, v41, v32
	v_cvt_pk_f16_f32 v126, v36, v37
	v_cvt_pk_f16_f32 v127, v38, v39
	ds_read_b64_tr_b16 v[140:141], v138 offset:27648
	ds_read_b64_tr_b16 v[142:143], v138 offset:28160
	v_add_f32_e32 v32, v42, v32
	v_add_f32_e32 v32, v43, v32
	v_add_f32_e32 v32, v44, v32
	v_add_f32_e32 v32, v45, v32
	v_cvt_pk_f16_f32 v120, v40, v41
	v_cvt_pk_f16_f32 v121, v42, v43
	ds_read_b64_tr_b16 v[136:137], v138 offset:31744
	ds_read_b64_tr_b16 v[138:139], v138 offset:32256
	v_add_f32_e32 v32, v46, v32
	v_add_f32_e32 v32, v47, v32
	v_add_f32_e32 v108, 0, v32
	v_cvt_pk_f16_f32 v122, v44, v45
	v_cvt_pk_f16_f32 v123, v46, v47
	s_nop 1
	s_nop 0
	v_add_f32_e32 v185, v185, v108
	v_max_f32_e32 v108, v81, v81
	v_max_f32_e32 v109, v80, v80
	v_max_f32_e32 v108, v109, v108
	v_max3_f32 v109, v82, v83, v65
	v_max3_f32 v108, v108, v64, v66
	v_max3_f32 v108, v108, v67, v84
	v_max3_f32 v109, v109, v86, v87
	v_max3_f32 v108, v108, v85, v68
	v_max3_f32 v109, v109, v70, v71
	v_max3_f32 v108, v108, v69, v88
	v_max3_f32 v109, v109, v90, v91
	v_max3_f32 v108, v108, v89, v72
	v_max3_f32 v109, v109, v74, v75
	ds_read_b128 v[48:51], v221 offset:32768
	ds_read_b128 v[32:35], v161 offset:32768
	ds_read_b128 v[52:55], v184 offset:32768
	ds_read_b128 v[36:39], v211 offset:32768
	ds_read_b128 v[56:59], v212 offset:32768
	ds_read_b128 v[40:43], v213 offset:32768
	ds_read_b128 v[60:63], v214 offset:32768
	ds_read_b128 v[44:47], v215 offset:32768
	v_max3_f32 v108, v108, v73, v92
	v_max3_f32 v109, v109, v94, v95
	v_max3_f32 v108, v108, v93, v76
	v_max3_f32 v109, v109, v78, v79
	v_max3_f32 v108, v108, v77, v109
	v_mov_b32_e32 v109, v108
	s_nop 1
	v_permlane32_swap_b32_e32 v108, v109
	v_max_f32_e32 v109, v109, v109
	v_max_f32_e32 v108, v108, v108
	v_max_f32_e32 v108, v108, v109
	v_fma_f32 v108, v108, s41, -v208
	v_cmp_lt_f32_e32 vcc, s29, v108
	s_cmp_lg_u64 vcc, 0
	s_cselect_b64 s[24:25], -1, 0
	s_cbranch_vccnz .LBB6_24

	.amdhsa_kernel _Z6k_attnILi1024ELi2048ELi1024ELi1024ELi2048ELi1024ELb1ELb1EEvPKDF16_S1_S1_PKfPDF16_
		.amdhsa_group_segment_fixed_size 0
		.amdhsa_private_segment_fixed_size 0
		.amdhsa_kernarg_size 40
		.amdhsa_user_sgpr_count 2
		.amdhsa_user_sgpr_dispatch_ptr 0
		.amdhsa_user_sgpr_queue_ptr 0
		.amdhsa_user_sgpr_kernarg_segment_ptr 1
		.amdhsa_user_sgpr_dispatch_id 0
		.amdhsa_user_sgpr_kernarg_preload_length 0
		.amdhsa_user_sgpr_kernarg_preload_offset 0
		.amdhsa_user_sgpr_private_segment_size 0
		.amdhsa_uses_dynamic_stack 0
		.amdhsa_enable_private_segment 0
		.amdhsa_system_sgpr_workgroup_id_x 1
		.amdhsa_system_sgpr_workgroup_id_y 0
		.amdhsa_system_sgpr_workgroup_id_z 0
		.amdhsa_system_sgpr_workgroup_info 0
		.amdhsa_system_vgpr_workitem_id 0
		.amdhsa_next_free_vgpr 240
		.amdhsa_next_free_sgpr 72
		.amdhsa_accum_offset 240
		.amdhsa_reserve_vcc 1
		.amdhsa_float_round_mode_32 0
		.amdhsa_float_round_mode_16_64 0
		.amdhsa_float_denorm_mode_32 3
		.amdhsa_float_denorm_mode_16_64 3
		.amdhsa_dx10_clamp 1
		.amdhsa_ieee_mode 1
		.amdhsa_fp16_overflow 0
		.amdhsa_tg_split 0
		.amdhsa_exception_fp_ieee_invalid_op 0
		.amdhsa_exception_fp_denorm_src 0
		.amdhsa_exception_fp_ieee_div_zero 0
		.amdhsa_exception_fp_ieee_overflow 0
		.amdhsa_exception_fp_ieee_underflow 0
		.amdhsa_exception_fp_ieee_inexact 0
		.amdhsa_exception_int_div_zero 0
	.end_amdhsa_kernel

amdhsa.kernels:
  - .agpr_count:     0
    .args:
      - .offset:         0
        .size:           384
        .value_kind:     by_value
    .group_segment_fixed_size: 5120
    .kernarg_segment_align: 8
    .kernarg_segment_size: 384
    .language:       OpenCL C
    .language_version:
      - 2
      - 0
    .max_flat_workgroup_size: 256
    .name:           _Z6k_prep6WtArgs
    .private_segment_fixed_size: 0
    .sgpr_count:     38
    .sgpr_spill_count: 0
    .symbol:         _Z6k_prep6WtArgs.kd
    .uniform_work_group_size: 1
    .uses_dynamic_stack: false
    .vgpr_count:     29
    .vgpr_spill_count: 0
    .wavefront_size: 64
  - .agpr_count:     0
    .args:
      - .actual_access:  read_only
        .address_space:  global
        .offset:         0
        .size:           8
        .value_kind:     global_buffer
      - .actual_access:  read_only
        .address_space:  global
        .offset:         8
        .size:           8
        .value_kind:     global_buffer
      - .actual_access:  read_only
        .address_space:  global
        .offset:         16
        .size:           8
        .value_kind:     global_buffer
      - .actual_access:  write_only
        .address_space:  global
        .offset:         24
        .size:           8
        .value_kind:     global_buffer
      - .actual_access:  write_only
        .address_space:  global
        .offset:         32
        .size:           8
        .value_kind:     global_buffer
      - .actual_access:  write_only
        .address_space:  global
        .offset:         40
        .size:           8
        .value_kind:     global_buffer
      - .offset:         48
        .size:           4
        .value_kind:     by_value
    .group_segment_fixed_size: 0
    .kernarg_segment_align: 8
    .kernarg_segment_size: 52
    .language:       OpenCL C
    .language_version:
      - 2
      - 0
    .max_flat_workgroup_size: 256
    .name:           _Z4k_lnPKDF16_PKfS2_PfPDF16_Phi
    .private_segment_fixed_size: 0
    .sgpr_count:     18
    .sgpr_spill_count: 0
    .symbol:         _Z4k_lnPKDF16_PKfS2_PfPDF16_Phi.kd
    .uniform_work_group_size: 1
    .uses_dynamic_stack: false
    .vgpr_count:     59
    .vgpr_spill_count: 0
    .wavefront_size: 64
  - .agpr_count:     0
    .args:
      - .offset:         0
        .size:           56
        .value_kind:     by_value
      - .offset:         56
        .size:           72
        .value_kind:     by_value
      - .offset:         128
        .size:           176
        .value_kind:     by_value
      - .address_space:  global
        .offset:         304
        .size:           8
        .value_kind:     global_buffer
      - .offset:         312
        .size:           4
        .value_kind:     hidden_block_count_x
      - .offset:         316
        .size:           4
        .value_kind:     hidden_block_count_y
      - .offset:         320
        .size:           4
        .value_kind:     hidden_block_count_z
      - .offset:         324
        .size:           2
        .value_kind:     hidden_group_size_x
      - .offset:         326
        .size:           2
        .value_kind:     hidden_group_size_y
      - .offset:         328
        .size:           2
        .value_kind:     hidden_group_size_z
      - .offset:         330
        .size:           2
        .value_kind:     hidden_remainder_x
      - .offset:         332
        .size:           2
        .value_kind:     hidden_remainder_y
      - .offset:         334
        .size:           2
        .value_kind:     hidden_remainder_z
      - .offset:         352
        .size:           8
        .value_kind:     hidden_global_offset_x
      - .offset:         360
        .size:           8
        .value_kind:     hidden_global_offset_y
      - .offset:         368
        .size:           8
        .value_kind:     hidden_global_offset_z
      - .offset:         376
        .size:           2
        .value_kind:     hidden_grid_dims
      - .offset:         432
        .size:           4
        .value_kind:     hidden_dynamic_lds_size
    .group_segment_fixed_size: 0
    .kernarg_segment_align: 8
    .kernarg_segment_size: 568
    .language:       OpenCL C
    .language_version:
      - 2
      - 0
    .max_flat_workgroup_size: 512
    .name:           _Z6k_gemmIN3pg84EpiHILi0ELb1EEELb1EEvNS0_4GemmET_6WtTailPj
    .private_segment_fixed_size: 0
    .sgpr_count:     78
    .sgpr_spill_count: 5
    .symbol:         _Z6k_gemmIN3pg84EpiHILi0ELb1EEELb1EEvNS0_4GemmET_6WtTailPj.kd
    .uniform_work_group_size: 1
    .uses_dynamic_stack: false
    .vgpr_count:     240
    .vgpr_spill_count: 0
    .wavefront_size: 64
  - .agpr_count:     0
    .args:
      - .address_space:  global
        .offset:         0
        .size:           8
        .value_kind:     global_buffer
      - .address_space:  global
        .offset:         8
        .size:           8
        .value_kind:     global_buffer
      - .address_space:  global
        .offset:         16
        .size:           8
        .value_kind:     global_buffer
      - .address_space:  global
        .offset:         24
        .size:           8
        .value_kind:     global_buffer
      - .address_space:  global
        .offset:         32
        .size:           8
        .value_kind:     global_buffer
    .group_segment_fixed_size: 0
    .kernarg_segment_align: 8
    .kernarg_segment_size: 40
    .language:       OpenCL C
    .language_version:
      - 2
      - 0
    .max_flat_workgroup_size: 512
    .name:           _Z6k_attnILi1024ELi1024ELi1024ELi1024ELi3072ELi1024ELb1ELb1EEvPKDF16_S1_S1_PKfPDF16_
    .private_segment_fixed_size: 0
    .sgpr_count:     55
    .sgpr_spill_count: 0
    .symbol:         _Z6k_attnILi1024ELi1024ELi1024ELi1024ELi3072ELi1024ELb1ELb1EEvPKDF16_S1_S1_PKfPDF16_.kd
    .uniform_work_group_size: 1
    .uses_dynamic_stack: false
    .vgpr_count:     224
    .vgpr_spill_count: 0
    .wavefront_size: 64
  - .agpr_count:     0
    .args:
      - .address_space:  global
        .offset:         0
        .size:           8
        .value_kind:     global_buffer
      - .address_space:  global
        .offset:         8
        .size:           8
        .value_kind:     global_buffer
      - .offset:         16
        .size:           4
        .value_kind:     by_value
      - .offset:         20
        .size:           4
        .value_kind:     by_value
      - .offset:         24
        .size:           4
        .value_kind:     by_value
      - .offset:         32
        .size:           32
        .value_kind:     by_value
    .group_segment_fixed_size: 0
    .kernarg_segment_align: 8
    .kernarg_segment_size: 64
    .language:       OpenCL C
    .language_version:
      - 2
      - 0
    .max_flat_workgroup_size: 512
    .name:           _ZN2g811k_gemm128f8INS_6EpiResEEEvPKhS3_iiiT_
    .private_segment_fixed_size: 0
    .sgpr_count:     34
    .sgpr_spill_count: 0
    .symbol:         _ZN2g811k_gemm128f8INS_6EpiResEEEvPKhS3_iiiT_.kd
    .uniform_work_group_size: 1
    .uses_dynamic_stack: false
    .vgpr_count:     98
    .vgpr_spill_count: 0
    .wavefront_size: 64
  - .agpr_count:     0
    .args:
      - .address_space:  global
        .offset:         0
        .size:           8
        .value_kind:     global_buffer
      - .address_space:  global
        .offset:         8
        .size:           8
        .value_kind:     global_buffer
      - .offset:         16
        .size:           4
        .value_kind:     by_value
      - .offset:         20
        .size:           4
        .value_kind:     by_value
      - .offset:         24
        .size:           4
        .value_kind:     by_value
      - .offset:         32
        .size:           16
        .value_kind:     by_value
    .group_segment_fixed_size: 0
    .kernarg_segment_align: 8
    .kernarg_segment_size: 48
    .language:       OpenCL C
    .language_version:
      - 2
      - 0
    .max_flat_workgroup_size: 512
    .name:           _ZN2g811k_gemm128f8INS_5EpiQ8EEEvPKhS3_iiiT_
    .private_segment_fixed_size: 0
    .sgpr_count:     78
    .sgpr_spill_count: 0
    .symbol:         _ZN2g811k_gemm128f8INS_5EpiQ8EEEvPKhS3_iiiT_.kd
    .uniform_work_group_size: 1
    .uses_dynamic_stack: false
    .vgpr_count:     240
    .vgpr_spill_count: 0
    .wavefront_size: 64
  - .agpr_count:     0
    .args:
      - .address_space:  global
        .offset:         0
        .size:           8
        .value_kind:     global_buffer
      - .address_space:  global
        .offset:         8
        .size:           8
        .value_kind:     global_buffer
      - .address_space:  global
        .offset:         16
        .size:           8
        .value_kind:     global_buffer
      - .address_space:  global
        .offset:         24
        .size:           8
        .value_kind:     global_buffer
      - .address_space:  global
        .offset:         32
        .size:           8
        .value_kind:     global_buffer
    .group_segment_fixed_size: 0
    .kernarg_segment_align: 8
    .kernarg_segment_size: 40
    .language:       OpenCL C
    .language_version:
      - 2
      - 0
    .max_flat_workgroup_size: 512
    .name:           _Z6k_attnILi1024ELi2048ELi1024ELi1024ELi2048ELi1024ELb1ELb1EEvPKDF16_S1_S1_PKfPDF16_
    .private_segment_fixed_size: 0
    .sgpr_count:     52
    .sgpr_spill_count: 0
    .symbol:         _Z6k_attnILi1024ELi2048ELi1024ELi1024ELi2048ELi1024ELb1ELb1EEvPKDF16_S1_S1_PKfPDF16_.kd
    .uniform_work_group_size: 1
    .uses_dynamic_stack: false
    .vgpr_count:     224
    .vgpr_spill_count: 0
    .wavefront_size: 64
  - .agpr_count:     0
    .args:
      - .offset:         0
        .size:           56
        .value_kind:     by_value
      - .offset:         56
        .size:           72
        .value_kind:     by_value
      - .offset:         128
        .size:           176
        .value_kind:     by_value
      - .address_space:  global
        .offset:         304
        .size:           8
        .value_kind:     global_buffer
      - .offset:         312
        .size:           4
        .value_kind:     hidden_block_count_x
      - .offset:         316
        .size:           4
        .value_kind:     hidden_block_count_y
      - .offset:         320
        .size:           4
        .value_kind:     hidden_block_count_z
      - .offset:         324
        .size:           2
        .value_kind:     hidden_group_size_x
      - .offset:         326
        .size:           2
        .value_kind:     hidden_group_size_y
      - .offset:         328
        .size:           2
        .value_kind:     hidden_group_size_z
      - .offset:         330
        .size:           2
        .value_kind:     hidden_remainder_x
      - .offset:         332
        .size:           2
        .value_kind:     hidden_remainder_y
      - .offset:         334
        .size:           2
        .value_kind:     hidden_remainder_z
      - .offset:         352
        .size:           8
        .value_kind:     hidden_global_offset_x
      - .offset:         360
        .size:           8
        .value_kind:     hidden_global_offset_y
      - .offset:         368
        .size:           8
        .value_kind:     hidden_global_offset_z
      - .offset:         376
        .size:           2
        .value_kind:     hidden_grid_dims
      - .offset:         432
        .size:           4
        .value_kind:     hidden_dynamic_lds_size
    .group_segment_fixed_size: 0
    .kernarg_segment_align: 8
    .kernarg_segment_size: 568
    .language:       OpenCL C
    .language_version:
      - 2
      - 0
    .max_flat_workgroup_size: 512
    .name:           _Z6k_gemmIN3pg84EpiHILi1ELb0EEELb0EEvNS0_4GemmET_6WtTailPj
    .private_segment_fixed_size: 0
    .sgpr_count:     85
    .sgpr_spill_count: 0
    .symbol:         _Z6k_gemmIN3pg84EpiHILi1ELb0EEELb0EEvNS0_4GemmET_6WtTailPj.kd
    .uniform_work_group_size: 1
    .uses_dynamic_stack: false
    .vgpr_count:     242
    .vgpr_spill_count: 0
    .wavefront_size: 64
  - .agpr_count:     0
    .args:
      - .address_space:  global
        .offset:         0
        .size:           8
        .value_kind:     global_buffer
      - .address_space:  global
        .offset:         8
        .size:           8
        .value_kind:     global_buffer
      - .offset:         16
        .size:           4
        .value_kind:     by_value
      - .offset:         20
        .size:           4
        .value_kind:     by_value
      - .offset:         24
        .size:           4
        .value_kind:     by_value
      - .offset:         32
        .size:           32
        .value_kind:     by_value
    .group_segment_fixed_size: 0
    .kernarg_segment_align: 8
    .kernarg_segment_size: 64
    .language:       OpenCL C
    .language_version:
      - 2
      - 0
    .max_flat_workgroup_size: 512
    .name:           _ZN4g1289k_gemm128INS_8EpiRes16EEEvPKDF16_S3_iiiT_
    .private_segment_fixed_size: 0
    .sgpr_count:     35
    .sgpr_spill_count: 0
    .symbol:         _ZN4g1289k_gemm128INS_8EpiRes16EEEvPKDF16_S3_iiiT_.kd
    .uniform_work_group_size: 1
    .uses_dynamic_stack: false
    .vgpr_count:     112
    .vgpr_spill_count: 0
    .wavefront_size: 64
